# cache policy: P3 hook and epilogue loads of the once-read 8-bit gates made non-temporal (on top of nt activation loads in P0)
# baseline (speedup 1.0000x reference)
;     static __device__ __forceinline__ float ub(unsigned w, int k) { return (float)((w >> (8 * k)) & 0xffu); }
;     __device__ __forceinline__ void mid(f32x4 (&acc)[2][2][4][2], const Unit& u, int b, int wr, int wc, int fr, int fq) const {
;         const unsigned char* pa = g8 + ((size_t)(b - 1) * cfg::MT + u.pm * BM + wr * 64 + fr) * cfg::DM + u.pn * BM + wc * 32 + 8 * fq; const unsigned char* pb = pa + (size_t)cfg::MT * cfg::DM;
;         u32x2 ga[16], gb[16];
; #pragma unroll
;         for (int i = 0; i < 16; ++i) { const size_t o = (size_t)(((i >> 3) & 1) * HALF + ((i >> 1) & 3) * 16) * cfg::DM + (i & 1) * HALF;
;             ga[i] = *(const u32x2*)(pa + o); gb[i] = *(const u32x2*)(pb + o); }
;         asm volatile("" ::: "memory");
; #pragma unroll
;         for (int i = 0; i < 16; ++i) { const int ai = (i >> 3) & 1, m = (i >> 1) & 3, bj = i & 1;
;             f32x4 r0, r1;
; #pragma unroll
;             for (int j = 0; j < 4; ++j) { r0[j] = ub(ga[i].x, j) * __builtin_amdgcn_rcpf(ub(gb[i].x, j)); r1[j] = ub(ga[i].y, j) * __builtin_amdgcn_rcpf(ub(gb[i].y, j)); }
;             acc[ai][bj][m][0] *= r0; acc[ai][bj][m][1] *= r1; }
.Lp3_hook_lead_done:
	s_lshr_b32 s2, s48, 4
	s_lshl_b64 s[12:13], s[2:3], 25
	s_add_u32 s12, s6, s12
	s_addc_u32 s13, s7, s13
	s_lshl_b32 s2, s24, 12
	s_lshl_b32 s30, s26, 8
	s_add_i32 s2, s2, s30
	s_lshl_b32 s30, s39, 3
	s_add_i32 s2, s2, s30
	s_addk_i32 s2, 0x1000
	s_add_u32 s12, s12, s2
	s_addc_u32 s13, s13, 0
	v_mbcnt_lo_u32_b32 v4, -1, 0
	v_mbcnt_hi_u32_b32 v4, -1, v4
	v_lshlrev_b32_e32 v4, 3, v4
	v_mov_b32_e32 v5, 0
	v_lshl_add_u64 v[222:223], s[12:13], 0, v[4:5]
	s_add_u32 s12, s12, 0xfe000000
	s_addc_u32 s13, s13, -1
	v_lshl_add_u64 v[4:5], s[12:13], 0, v[4:5]
	global_load_dwordx2 v[192:193], v[4:5], off offset:-4096 nt
	global_load_dwordx2 v[194:195], v[222:223], off offset:-4096 nt
	global_load_dwordx2 v[214:215], v[4:5], off offset:-3584 nt
	global_load_dwordx2 v[216:217], v[222:223], off offset:-3584 nt
	global_load_dwordx2 v[210:211], v[4:5], off offset:-3072 nt
	global_load_dwordx2 v[212:213], v[222:223], off offset:-3072 nt
	global_load_dwordx2 v[206:207], v[4:5], off offset:-2560 nt
	global_load_dwordx2 v[208:209], v[222:223], off offset:-2560 nt
	global_load_dwordx2 v[202:203], v[4:5], off offset:-2048 nt
	global_load_dwordx2 v[204:205], v[222:223], off offset:-2048 nt
	global_load_dwordx2 v[198:199], v[4:5], off offset:-1536 nt
	global_load_dwordx2 v[200:201], v[222:223], off offset:-1536 nt
	global_load_dwordx2 v[190:191], v[4:5], off offset:-1024 nt
	global_load_dwordx2 v[196:197], v[222:223], off offset:-1024 nt
	global_load_dwordx2 v[186:187], v[4:5], off offset:-512 nt
	global_load_dwordx2 v[188:189], v[222:223], off offset:-512 nt
	global_load_dwordx2 v[182:183], v[4:5], off nt
	global_load_dwordx2 v[184:185], v[222:223], off nt
	global_load_dwordx2 v[178:179], v[4:5], off offset:512 nt
	global_load_dwordx2 v[180:181], v[222:223], off offset:512 nt
	global_load_dwordx2 v[174:175], v[4:5], off offset:1024 nt
	global_load_dwordx2 v[176:177], v[222:223], off offset:1024 nt
	global_load_dwordx2 v[170:171], v[4:5], off offset:1536 nt
	global_load_dwordx2 v[172:173], v[222:223], off offset:1536 nt
	global_load_dwordx2 v[166:167], v[4:5], off offset:2048 nt
	global_load_dwordx2 v[168:169], v[222:223], off offset:2048 nt
	global_load_dwordx2 v[162:163], v[4:5], off offset:2560 nt
	global_load_dwordx2 v[164:165], v[222:223], off offset:2560 nt
	global_load_dwordx2 v[158:159], v[4:5], off offset:3072 nt
	global_load_dwordx2 v[160:161], v[222:223], off offset:3072 nt
	global_load_dwordx2 v[156:157], v[222:223], off offset:3584 nt
	global_load_dwordx2 v[4:5], v[4:5], off offset:3584 nt
	s_waitcnt vmcnt(28)
	v_cvt_f32_ubyte3_e32 v239, v192
	v_cvt_f32_ubyte0_e32 v2, v194
	v_cvt_f32_ubyte2_e32 v238, v192
	v_cvt_f32_ubyte1_e32 v245, v192
	v_cvt_f32_ubyte0_e32 v244, v192
	v_rcp_iflag_f32_e32 v222, v2
	v_cvt_f32_ubyte0_e32 v2, v195
	v_rcp_iflag_f32_e32 v232, v2
	v_cvt_f32_ubyte1_e32 v2, v194
	v_rcp_iflag_f32_e32 v223, v2
	v_cvt_f32_ubyte1_e32 v2, v195
	v_rcp_iflag_f32_e32 v233, v2
	v_cvt_f32_ubyte2_e32 v2, v194
	v_rcp_iflag_f32_e32 v234, v2
	v_cvt_f32_ubyte2_e32 v2, v195
	v_rcp_iflag_f32_e32 v236, v2
	v_cvt_f32_ubyte3_e32 v2, v194
	v_rcp_iflag_f32_e32 v235, v2
	v_cvt_f32_ubyte3_e32 v2, v195
	v_rcp_iflag_f32_e32 v237, v2
	v_cvt_f32_ubyte3_e32 v195, v193
	v_pk_mul_f32 v[234:235], v[234:235], v[238:239]
	v_cvt_f32_ubyte1_e32 v239, v193
	v_cvt_f32_ubyte0_e32 v238, v193
	v_cvt_f32_ubyte2_e32 v194, v193
	v_pk_mul_f32 v[192:193], v[232:233], v[238:239]
	v_cvt_f32_ubyte0_e32 v2, v216
	v_pk_mul_f32 v[194:195], v[236:237], v[194:195]
	v_pk_mul_f32 v[126:127], v[126:127], v[192:193]
	v_rcp_iflag_f32_e32 v192, v2
	v_cvt_f32_ubyte0_e32 v2, v217
	v_pk_mul_f32 v[128:129], v[128:129], v[194:195]
	v_rcp_iflag_f32_e32 v194, v2
	v_cvt_f32_ubyte1_e32 v2, v216
	v_rcp_iflag_f32_e32 v193, v2
	v_cvt_f32_ubyte1_e32 v2, v217
	v_pk_mul_f32 v[222:223], v[222:223], v[244:245]
	v_rcp_iflag_f32_e32 v195, v2
	v_cvt_f32_ubyte2_e32 v2, v216
	v_pk_mul_f32 v[130:131], v[130:131], v[222:223]
	v_rcp_iflag_f32_e32 v222, v2
	v_cvt_f32_ubyte2_e32 v2, v217
	v_rcp_iflag_f32_e32 v232, v2
	v_cvt_f32_ubyte3_e32 v2, v216
	v_rcp_iflag_f32_e32 v223, v2
	v_pk_mul_f32 v[132:133], v[132:133], v[234:235]
	v_cvt_f32_ubyte3_e32 v235, v214
	v_cvt_f32_ubyte2_e32 v234, v214
	v_cvt_f32_ubyte1_e32 v237, v214
	v_cvt_f32_ubyte0_e32 v236, v214
	v_cvt_f32_ubyte3_e32 v2, v217
	v_pk_mul_f32 v[192:193], v[192:193], v[236:237]
	v_pk_mul_f32 v[222:223], v[222:223], v[234:235]
	v_rcp_iflag_f32_e32 v233, v2
	v_cvt_f32_ubyte1_e32 v235, v215
	v_cvt_f32_ubyte0_e32 v234, v215
	s_waitcnt vmcnt(0)
;     static __device__ __forceinline__ float ub(unsigned w, int k) { return (float)((w >> (8 * k)) & 0xffu); }
;     __device__ __forceinline__ void mid(f32x4 (&acc)[2][2][4][2], const Unit& u, int b, int wr, int wc, int fr, int fq) const {
;     ...
;         for (int i = 0; i < 16; ++i) { const int ai = (i >> 3) & 1, m = (i >> 1) & 3, bj = i & 1;
;             f32x4 r0, r1;
; #pragma unroll
;             for (int j = 0; j < 4; ++j) { r0[j] = ub(ga[i].x, j) * __builtin_amdgcn_rcpf(ub(gb[i].x, j)); r1[j] = ub(ga[i].y, j) * __builtin_amdgcn_rcpf(ub(gb[i].y, j)); }
;             acc[ai][bj][m][0] *= r0; acc[ai][bj][m][1] *= r1; }
	v_cvt_f32_ubyte0_e32 v2, v212
	v_pk_mul_f32 v[194:195], v[194:195], v[234:235]
	v_pk_mul_f32 v[122:123], v[122:123], v[192:193]
	v_rcp_iflag_f32_e32 v192, v2
	v_cvt_f32_ubyte0_e32 v2, v213
	v_pk_mul_f32 v[118:119], v[118:119], v[194:195]
	v_rcp_iflag_f32_e32 v194, v2
	v_cvt_f32_ubyte1_e32 v2, v212
	v_cvt_f32_ubyte3_e32 v217, v215
	v_cvt_f32_ubyte2_e32 v216, v215
	v_rcp_iflag_f32_e32 v193, v2
	v_cvt_f32_ubyte1_e32 v2, v213
	v_pk_mul_f32 v[214:215], v[232:233], v[216:217]
	v_rcp_iflag_f32_e32 v195, v2
	v_cvt_f32_ubyte2_e32 v2, v212
	v_pk_mul_f32 v[120:121], v[120:121], v[214:215]
	v_rcp_iflag_f32_e32 v214, v2
	v_cvt_f32_ubyte2_e32 v2, v213
	v_rcp_iflag_f32_e32 v216, v2
	v_cvt_f32_ubyte3_e32 v2, v212
	v_rcp_iflag_f32_e32 v215, v2
	v_pk_mul_f32 v[124:125], v[124:125], v[222:223]
	v_cvt_f32_ubyte3_e32 v223, v210
	v_cvt_f32_ubyte2_e32 v222, v210
	v_cvt_f32_ubyte1_e32 v233, v210
	v_cvt_f32_ubyte0_e32 v232, v210
	v_cvt_f32_ubyte3_e32 v2, v213
	v_pk_mul_f32 v[192:193], v[192:193], v[232:233]
	v_pk_mul_f32 v[214:215], v[214:215], v[222:223]
	v_rcp_iflag_f32_e32 v217, v2
	v_cvt_f32_ubyte1_e32 v223, v211
	v_cvt_f32_ubyte0_e32 v222, v211
	v_cvt_f32_ubyte0_e32 v2, v208
	v_pk_mul_f32 v[194:195], v[194:195], v[222:223]
	v_pk_mul_f32 v[114:115], v[114:115], v[192:193]
	v_rcp_iflag_f32_e32 v192, v2
	v_cvt_f32_ubyte0_e32 v2, v209
	v_pk_mul_f32 v[110:111], v[110:111], v[194:195]
	v_rcp_iflag_f32_e32 v194, v2
	v_cvt_f32_ubyte1_e32 v2, v208
	v_cvt_f32_ubyte3_e32 v213, v211
	v_cvt_f32_ubyte2_e32 v212, v211
	v_rcp_iflag_f32_e32 v193, v2
	v_cvt_f32_ubyte1_e32 v2, v209
	v_pk_mul_f32 v[210:211], v[216:217], v[212:213]
	v_rcp_iflag_f32_e32 v195, v2
	v_cvt_f32_ubyte2_e32 v2, v208
	v_pk_mul_f32 v[112:113], v[112:113], v[210:211]
	v_rcp_iflag_f32_e32 v210, v2
	v_cvt_f32_ubyte2_e32 v2, v209
	v_rcp_iflag_f32_e32 v212, v2
	v_cvt_f32_ubyte3_e32 v2, v208
	v_rcp_iflag_f32_e32 v211, v2
	v_pk_mul_f32 v[116:117], v[116:117], v[214:215]
	v_cvt_f32_ubyte3_e32 v215, v206
	v_cvt_f32_ubyte2_e32 v214, v206
	v_cvt_f32_ubyte1_e32 v217, v206
	v_cvt_f32_ubyte0_e32 v216, v206
	v_cvt_f32_ubyte3_e32 v2, v209
	v_pk_mul_f32 v[192:193], v[192:193], v[216:217]
	v_pk_mul_f32 v[210:211], v[210:211], v[214:215]
	v_rcp_iflag_f32_e32 v213, v2
	v_cvt_f32_ubyte1_e32 v215, v207
	v_cvt_f32_ubyte0_e32 v214, v207
	v_cvt_f32_ubyte0_e32 v2, v204
	v_pk_mul_f32 v[194:195], v[194:195], v[214:215]
	v_pk_mul_f32 v[106:107], v[106:107], v[192:193]
	v_rcp_iflag_f32_e32 v192, v2
	v_cvt_f32_ubyte0_e32 v2, v205
	v_pk_mul_f32 v[102:103], v[102:103], v[194:195]
	v_rcp_iflag_f32_e32 v194, v2
	v_cvt_f32_ubyte1_e32 v2, v204
	v_cvt_f32_ubyte3_e32 v209, v207
	v_cvt_f32_ubyte2_e32 v208, v207
	v_rcp_iflag_f32_e32 v193, v2
	v_cvt_f32_ubyte1_e32 v2, v205
	v_pk_mul_f32 v[206:207], v[212:213], v[208:209]
	v_rcp_iflag_f32_e32 v195, v2
	v_cvt_f32_ubyte2_e32 v2, v204
	v_pk_mul_f32 v[104:105], v[104:105], v[206:207]
	v_rcp_iflag_f32_e32 v206, v2
	v_cvt_f32_ubyte2_e32 v2, v205
	v_rcp_iflag_f32_e32 v208, v2
	v_cvt_f32_ubyte3_e32 v2, v204
	v_rcp_iflag_f32_e32 v207, v2
	v_pk_mul_f32 v[108:109], v[108:109], v[210:211]
	v_cvt_f32_ubyte3_e32 v211, v202
	v_cvt_f32_ubyte2_e32 v210, v202
	v_cvt_f32_ubyte1_e32 v213, v202
	v_cvt_f32_ubyte0_e32 v212, v202
	v_cvt_f32_ubyte3_e32 v2, v205
	v_pk_mul_f32 v[192:193], v[192:193], v[212:213]
	v_pk_mul_f32 v[206:207], v[206:207], v[210:211]
	v_rcp_iflag_f32_e32 v209, v2
	v_cvt_f32_ubyte1_e32 v211, v203
	v_cvt_f32_ubyte0_e32 v210, v203
	v_cvt_f32_ubyte0_e32 v2, v200
	v_pk_mul_f32 v[194:195], v[194:195], v[210:211]
	v_pk_mul_f32 v[98:99], v[98:99], v[192:193]
	v_rcp_iflag_f32_e32 v192, v2
	v_cvt_f32_ubyte0_e32 v2, v201
	v_pk_mul_f32 v[94:95], v[94:95], v[194:195]
	v_rcp_iflag_f32_e32 v194, v2
	v_cvt_f32_ubyte1_e32 v2, v200
	v_cvt_f32_ubyte3_e32 v205, v203
	v_cvt_f32_ubyte2_e32 v204, v203
	v_rcp_iflag_f32_e32 v193, v2
	v_cvt_f32_ubyte1_e32 v2, v201
	v_pk_mul_f32 v[202:203], v[208:209], v[204:205]
	v_rcp_iflag_f32_e32 v195, v2
	v_cvt_f32_ubyte2_e32 v2, v200
	v_pk_mul_f32 v[96:97], v[96:97], v[202:203]
	v_rcp_iflag_f32_e32 v202, v2
	v_cvt_f32_ubyte2_e32 v2, v201
	v_rcp_iflag_f32_e32 v204, v2
	v_cvt_f32_ubyte3_e32 v2, v200
	v_rcp_iflag_f32_e32 v203, v2
	v_pk_mul_f32 v[100:101], v[100:101], v[206:207]
	v_cvt_f32_ubyte3_e32 v207, v198
	v_cvt_f32_ubyte2_e32 v206, v198
	v_cvt_f32_ubyte1_e32 v209, v198
	v_cvt_f32_ubyte0_e32 v208, v198
	v_cvt_f32_ubyte3_e32 v2, v201
	v_pk_mul_f32 v[192:193], v[192:193], v[208:209]
	v_pk_mul_f32 v[202:203], v[202:203], v[206:207]
	v_rcp_iflag_f32_e32 v205, v2
	v_cvt_f32_ubyte1_e32 v207, v199
	v_cvt_f32_ubyte0_e32 v206, v199
	v_cvt_f32_ubyte0_e32 v2, v196
	v_pk_mul_f32 v[194:195], v[194:195], v[206:207]
	v_pk_mul_f32 v[90:91], v[90:91], v[192:193]
	v_rcp_iflag_f32_e32 v192, v2
	v_cvt_f32_ubyte0_e32 v2, v197
	v_pk_mul_f32 v[86:87], v[86:87], v[194:195]
	v_rcp_iflag_f32_e32 v194, v2
	v_cvt_f32_ubyte1_e32 v2, v196
	v_cvt_f32_ubyte3_e32 v201, v199
	v_cvt_f32_ubyte2_e32 v200, v199
	v_rcp_iflag_f32_e32 v193, v2
	v_cvt_f32_ubyte1_e32 v2, v197
	v_pk_mul_f32 v[198:199], v[204:205], v[200:201]
	v_rcp_iflag_f32_e32 v195, v2
	v_cvt_f32_ubyte2_e32 v2, v196
	v_pk_mul_f32 v[88:89], v[88:89], v[198:199]
	v_rcp_iflag_f32_e32 v198, v2
	v_cvt_f32_ubyte2_e32 v2, v197
	v_rcp_iflag_f32_e32 v200, v2
	v_cvt_f32_ubyte3_e32 v2, v196
	v_rcp_iflag_f32_e32 v199, v2
	v_pk_mul_f32 v[92:93], v[92:93], v[202:203]
	v_cvt_f32_ubyte3_e32 v203, v190
	v_cvt_f32_ubyte2_e32 v202, v190
	v_pk_mul_f32 v[198:199], v[198:199], v[202:203]
	v_cvt_f32_ubyte3_e32 v2, v197
	v_cvt_f32_ubyte1_e32 v203, v191
	v_cvt_f32_ubyte0_e32 v202, v191
	v_cvt_f32_ubyte1_e32 v205, v190
	v_cvt_f32_ubyte0_e32 v204, v190
	v_rcp_iflag_f32_e32 v201, v2
;     static __device__ __forceinline__ float ub(unsigned w, int k) { return (float)((w >> (8 * k)) & 0xffu); }
;     __device__ __forceinline__ void mid(f32x4 (&acc)[2][2][4][2], const Unit& u, int b, int wr, int wc, int fr, int fq) const {
;     ...
;         for (int i = 0; i < 16; ++i) { const int ai = (i >> 3) & 1, m = (i >> 1) & 3, bj = i & 1;
;             f32x4 r0, r1;
; #pragma unroll
;             for (int j = 0; j < 4; ++j) { r0[j] = ub(ga[i].x, j) * __builtin_amdgcn_rcpf(ub(gb[i].x, j)); r1[j] = ub(ga[i].y, j) * __builtin_amdgcn_rcpf(ub(gb[i].y, j)); }
;             acc[ai][bj][m][0] *= r0; acc[ai][bj][m][1] *= r1; }
	v_cvt_f32_ubyte3_e32 v197, v191
	v_cvt_f32_ubyte2_e32 v196, v191
	v_pk_mul_f32 v[190:191], v[194:195], v[202:203]
	v_cvt_f32_ubyte0_e32 v2, v188
	v_pk_mul_f32 v[192:193], v[192:193], v[204:205]
	v_pk_mul_f32 v[78:79], v[78:79], v[190:191]
	v_rcp_iflag_f32_e32 v190, v2
	v_cvt_f32_ubyte0_e32 v2, v189
	v_pk_mul_f32 v[82:83], v[82:83], v[192:193]
	v_rcp_iflag_f32_e32 v192, v2
	v_cvt_f32_ubyte1_e32 v2, v188
	v_rcp_iflag_f32_e32 v191, v2
	v_cvt_f32_ubyte1_e32 v2, v189
	v_pk_mul_f32 v[194:195], v[200:201], v[196:197]
	v_rcp_iflag_f32_e32 v193, v2
	v_cvt_f32_ubyte2_e32 v2, v188
	v_pk_mul_f32 v[80:81], v[80:81], v[194:195]
	v_rcp_iflag_f32_e32 v194, v2
	v_cvt_f32_ubyte2_e32 v2, v189
	v_rcp_iflag_f32_e32 v196, v2
	v_cvt_f32_ubyte3_e32 v2, v188
	v_rcp_iflag_f32_e32 v195, v2
	v_cvt_f32_ubyte3_e32 v2, v189
	v_rcp_iflag_f32_e32 v197, v2
	v_pk_mul_f32 v[84:85], v[84:85], v[198:199]
	v_cvt_f32_ubyte3_e32 v199, v186
	v_cvt_f32_ubyte2_e32 v198, v186
	v_pk_mul_f32 v[194:195], v[194:195], v[198:199]
	v_cvt_f32_ubyte1_e32 v199, v187
	v_cvt_f32_ubyte0_e32 v198, v187
	v_cvt_f32_ubyte1_e32 v201, v186
	v_cvt_f32_ubyte0_e32 v200, v186
	v_cvt_f32_ubyte3_e32 v189, v187
	v_cvt_f32_ubyte2_e32 v188, v187
	v_pk_mul_f32 v[186:187], v[192:193], v[198:199]
	v_cvt_f32_ubyte0_e32 v2, v184
	v_pk_mul_f32 v[188:189], v[196:197], v[188:189]
	v_pk_mul_f32 v[70:71], v[70:71], v[186:187]
	v_rcp_iflag_f32_e32 v186, v2
	v_cvt_f32_ubyte0_e32 v2, v185
	v_pk_mul_f32 v[72:73], v[72:73], v[188:189]
	v_rcp_iflag_f32_e32 v188, v2
	v_cvt_f32_ubyte1_e32 v2, v184
	v_rcp_iflag_f32_e32 v187, v2
	v_cvt_f32_ubyte1_e32 v2, v185
	v_pk_mul_f32 v[190:191], v[190:191], v[200:201]
	v_rcp_iflag_f32_e32 v189, v2
	v_cvt_f32_ubyte2_e32 v2, v184
	v_pk_mul_f32 v[74:75], v[74:75], v[190:191]
	v_rcp_iflag_f32_e32 v190, v2
	v_cvt_f32_ubyte2_e32 v2, v185
	v_rcp_iflag_f32_e32 v192, v2
	v_cvt_f32_ubyte3_e32 v2, v184
	v_rcp_iflag_f32_e32 v191, v2
	v_cvt_f32_ubyte3_e32 v2, v185
	v_rcp_iflag_f32_e32 v193, v2
	v_pk_mul_f32 v[76:77], v[76:77], v[194:195]
	v_cvt_f32_ubyte3_e32 v195, v182
	v_cvt_f32_ubyte2_e32 v194, v182
	v_pk_mul_f32 v[190:191], v[190:191], v[194:195]
	v_cvt_f32_ubyte1_e32 v195, v183
	v_cvt_f32_ubyte0_e32 v194, v183
	v_cvt_f32_ubyte1_e32 v197, v182
	v_cvt_f32_ubyte0_e32 v196, v182
	v_cvt_f32_ubyte3_e32 v185, v183
	v_cvt_f32_ubyte2_e32 v184, v183
	v_pk_mul_f32 v[182:183], v[188:189], v[194:195]
	v_cvt_f32_ubyte0_e32 v2, v180
	v_pk_mul_f32 v[184:185], v[192:193], v[184:185]
	v_pk_mul_f32 v[62:63], v[62:63], v[182:183]
	v_rcp_iflag_f32_e32 v182, v2
	v_cvt_f32_ubyte0_e32 v2, v181
	v_pk_mul_f32 v[64:65], v[64:65], v[184:185]
	v_rcp_iflag_f32_e32 v184, v2
	v_cvt_f32_ubyte1_e32 v2, v180
	v_rcp_iflag_f32_e32 v183, v2
	v_cvt_f32_ubyte1_e32 v2, v181
	v_pk_mul_f32 v[186:187], v[186:187], v[196:197]
	v_rcp_iflag_f32_e32 v185, v2
	v_cvt_f32_ubyte2_e32 v2, v180
	v_pk_mul_f32 v[66:67], v[66:67], v[186:187]
	v_rcp_iflag_f32_e32 v186, v2
	v_cvt_f32_ubyte2_e32 v2, v181
	v_rcp_iflag_f32_e32 v188, v2
	v_cvt_f32_ubyte3_e32 v2, v180
	v_rcp_iflag_f32_e32 v187, v2
	v_cvt_f32_ubyte3_e32 v2, v181
	v_rcp_iflag_f32_e32 v189, v2
	v_pk_mul_f32 v[68:69], v[68:69], v[190:191]
	v_cvt_f32_ubyte3_e32 v191, v178
	v_cvt_f32_ubyte2_e32 v190, v178
	v_pk_mul_f32 v[186:187], v[186:187], v[190:191]
	v_cvt_f32_ubyte1_e32 v191, v179
	v_cvt_f32_ubyte0_e32 v190, v179
	v_cvt_f32_ubyte1_e32 v193, v178
	v_cvt_f32_ubyte0_e32 v192, v178
	v_cvt_f32_ubyte3_e32 v181, v179
	v_cvt_f32_ubyte2_e32 v180, v179
	v_pk_mul_f32 v[178:179], v[184:185], v[190:191]
	v_cvt_f32_ubyte0_e32 v2, v176
	v_pk_mul_f32 v[180:181], v[188:189], v[180:181]
	v_pk_mul_f32 v[54:55], v[54:55], v[178:179]
	v_rcp_iflag_f32_e32 v178, v2
	v_cvt_f32_ubyte0_e32 v2, v177
	v_pk_mul_f32 v[56:57], v[56:57], v[180:181]
	v_rcp_iflag_f32_e32 v180, v2
	v_cvt_f32_ubyte1_e32 v2, v176
	v_rcp_iflag_f32_e32 v179, v2
	v_cvt_f32_ubyte1_e32 v2, v177
	v_pk_mul_f32 v[182:183], v[182:183], v[192:193]
	v_rcp_iflag_f32_e32 v181, v2
	v_cvt_f32_ubyte2_e32 v2, v176
	v_pk_mul_f32 v[58:59], v[58:59], v[182:183]
	v_rcp_iflag_f32_e32 v182, v2
	v_cvt_f32_ubyte2_e32 v2, v177
	v_rcp_iflag_f32_e32 v184, v2
	v_cvt_f32_ubyte3_e32 v2, v176
	v_rcp_iflag_f32_e32 v183, v2
	v_cvt_f32_ubyte3_e32 v2, v177
	v_rcp_iflag_f32_e32 v185, v2
	v_pk_mul_f32 v[60:61], v[60:61], v[186:187]
	v_cvt_f32_ubyte3_e32 v187, v174
	v_cvt_f32_ubyte2_e32 v186, v174
	v_pk_mul_f32 v[182:183], v[182:183], v[186:187]
	v_cvt_f32_ubyte1_e32 v187, v175
	v_cvt_f32_ubyte0_e32 v186, v175
	v_cvt_f32_ubyte1_e32 v189, v174
	v_cvt_f32_ubyte0_e32 v188, v174
	v_cvt_f32_ubyte3_e32 v177, v175
	v_cvt_f32_ubyte2_e32 v176, v175
	v_pk_mul_f32 v[174:175], v[180:181], v[186:187]
	v_cvt_f32_ubyte0_e32 v2, v172
	v_pk_mul_f32 v[176:177], v[184:185], v[176:177]
	v_pk_mul_f32 v[46:47], v[46:47], v[174:175]
	v_rcp_iflag_f32_e32 v174, v2
	v_cvt_f32_ubyte0_e32 v2, v173
	v_pk_mul_f32 v[48:49], v[48:49], v[176:177]
	v_rcp_iflag_f32_e32 v176, v2
	v_cvt_f32_ubyte1_e32 v2, v172
	v_rcp_iflag_f32_e32 v175, v2
	v_cvt_f32_ubyte1_e32 v2, v173
	v_pk_mul_f32 v[178:179], v[178:179], v[188:189]
	v_rcp_iflag_f32_e32 v177, v2
	v_cvt_f32_ubyte2_e32 v2, v172
	v_pk_mul_f32 v[50:51], v[50:51], v[178:179]
	v_rcp_iflag_f32_e32 v178, v2
	v_cvt_f32_ubyte2_e32 v2, v173
	v_rcp_iflag_f32_e32 v180, v2
	v_cvt_f32_ubyte3_e32 v2, v172
	v_rcp_iflag_f32_e32 v179, v2
;     static __device__ __forceinline__ float ub(unsigned w, int k) { return (float)((w >> (8 * k)) & 0xffu); }
; #define PG8_MMA(ai, bj, At, Bt) do { __builtin_amdgcn_s_setprio(1); _Pragma("unroll") for (int m = 0; m < 4; ++m) _Pragma("unroll") for (int n = 0; n < 2; ++n) _Pragma("unroll") for (int k = 0; k < 2; ++k) \
;         acc[ai][bj][m][n] = __builtin_amdgcn_mfma_f32_16x16x32_bf16(Bt[n][k], At[m][k], acc[ai][bj][m][n], 0, 0, 0); __builtin_amdgcn_s_setprio(0); } while (0)
; #define PG8_WAIT_V(n) asm volatile("s_waitcnt vmcnt(" #n ")" ::: "memory")
; #define PG8_WAIT_L(n) asm volatile("s_waitcnt lgkmcnt(" #n ")" ::: "memory")
; #define PG8_BAR __builtin_amdgcn_s_barrier()
; #define PG8_SCHED __builtin_amdgcn_sched_barrier(0)
;     __device__ __forceinline__ void mid(f32x4 (&acc)[2][2][4][2], const Unit& u, int b, int wr, int wc, int fr, int fq) const {
;     ...
;         for (int i = 0; i < 16; ++i) { const int ai = (i >> 3) & 1, m = (i >> 1) & 3, bj = i & 1;
;             f32x4 r0, r1;
; #pragma unroll
;             for (int j = 0; j < 4; ++j) { r0[j] = ub(ga[i].x, j) * __builtin_amdgcn_rcpf(ub(gb[i].x, j)); r1[j] = ub(ga[i].y, j) * __builtin_amdgcn_rcpf(ub(gb[i].y, j)); }
;             acc[ai][bj][m][0] *= r0; acc[ai][bj][m][1] *= r1; }
; template <class Epi, class Sched, bool ALIGN_EPI = false, bool SP2 = false>
; __device__ __forceinline__ void gemm_phase(PG8_LAS unsigned char* lds, const Gemm g, const Sched& S, const Epi& E) {
;     ...
;             PG8_WAIT_V(8); PG8_WAIT_L(0); PG8_BAR; PG8_MMA(0, 0, At, B0); PG8_MMA(0, 1, At, B1); PG8_BAR; PG8_SCHED;
	v_cvt_f32_ubyte3_e32 v2, v173
	v_rcp_iflag_f32_e32 v181, v2
	v_pk_mul_f32 v[52:53], v[52:53], v[182:183]
	v_cvt_f32_ubyte3_e32 v183, v170
	v_cvt_f32_ubyte2_e32 v182, v170
	v_pk_mul_f32 v[178:179], v[178:179], v[182:183]
	v_cvt_f32_ubyte1_e32 v183, v171
	v_cvt_f32_ubyte0_e32 v182, v171
	v_cvt_f32_ubyte1_e32 v185, v170
	v_cvt_f32_ubyte0_e32 v184, v170
	v_cvt_f32_ubyte3_e32 v173, v171
	v_cvt_f32_ubyte2_e32 v172, v171
	v_pk_mul_f32 v[170:171], v[176:177], v[182:183]
	v_cvt_f32_ubyte0_e32 v2, v168
	v_pk_mul_f32 v[172:173], v[180:181], v[172:173]
	v_pk_mul_f32 v[38:39], v[38:39], v[170:171]
	v_rcp_iflag_f32_e32 v170, v2
	v_cvt_f32_ubyte0_e32 v2, v169
	v_pk_mul_f32 v[40:41], v[40:41], v[172:173]
	v_rcp_iflag_f32_e32 v172, v2
	v_cvt_f32_ubyte1_e32 v2, v168
	v_rcp_iflag_f32_e32 v171, v2
	v_cvt_f32_ubyte1_e32 v2, v169
	v_pk_mul_f32 v[174:175], v[174:175], v[184:185]
	v_rcp_iflag_f32_e32 v173, v2
	v_cvt_f32_ubyte2_e32 v2, v168
	v_pk_mul_f32 v[42:43], v[42:43], v[174:175]
	v_rcp_iflag_f32_e32 v174, v2
	v_cvt_f32_ubyte2_e32 v2, v169
	v_rcp_iflag_f32_e32 v176, v2
	v_cvt_f32_ubyte3_e32 v2, v168
	v_rcp_iflag_f32_e32 v175, v2
	v_cvt_f32_ubyte3_e32 v2, v169
	v_rcp_iflag_f32_e32 v177, v2
	v_pk_mul_f32 v[44:45], v[44:45], v[178:179]
	v_cvt_f32_ubyte3_e32 v179, v166
	v_cvt_f32_ubyte2_e32 v178, v166
	v_pk_mul_f32 v[174:175], v[174:175], v[178:179]
	v_cvt_f32_ubyte1_e32 v179, v167
	v_cvt_f32_ubyte0_e32 v178, v167
	v_cvt_f32_ubyte1_e32 v181, v166
	v_cvt_f32_ubyte0_e32 v180, v166
	v_cvt_f32_ubyte3_e32 v169, v167
	v_cvt_f32_ubyte2_e32 v168, v167
	v_pk_mul_f32 v[166:167], v[172:173], v[178:179]
	v_cvt_f32_ubyte0_e32 v2, v164
	v_pk_mul_f32 v[168:169], v[176:177], v[168:169]
	v_pk_mul_f32 v[30:31], v[30:31], v[166:167]
	v_rcp_iflag_f32_e32 v166, v2
	v_cvt_f32_ubyte0_e32 v2, v165
	v_pk_mul_f32 v[32:33], v[32:33], v[168:169]
	v_rcp_iflag_f32_e32 v168, v2
	v_cvt_f32_ubyte1_e32 v2, v164
	v_rcp_iflag_f32_e32 v167, v2
	v_cvt_f32_ubyte1_e32 v2, v165
	v_pk_mul_f32 v[170:171], v[170:171], v[180:181]
	v_rcp_iflag_f32_e32 v169, v2
	v_cvt_f32_ubyte2_e32 v2, v164
	v_pk_mul_f32 v[34:35], v[34:35], v[170:171]
	v_rcp_iflag_f32_e32 v170, v2
	v_cvt_f32_ubyte2_e32 v2, v165
	v_rcp_iflag_f32_e32 v172, v2
	v_cvt_f32_ubyte3_e32 v2, v164
	v_rcp_iflag_f32_e32 v171, v2
	v_cvt_f32_ubyte3_e32 v2, v165
	v_rcp_iflag_f32_e32 v173, v2
	v_pk_mul_f32 v[36:37], v[36:37], v[174:175]
	v_cvt_f32_ubyte3_e32 v175, v162
	v_cvt_f32_ubyte2_e32 v174, v162
	v_pk_mul_f32 v[170:171], v[170:171], v[174:175]
	v_cvt_f32_ubyte1_e32 v175, v163
	v_cvt_f32_ubyte0_e32 v174, v163
	v_cvt_f32_ubyte1_e32 v177, v162
	v_cvt_f32_ubyte0_e32 v176, v162
	v_cvt_f32_ubyte3_e32 v165, v163
	v_cvt_f32_ubyte2_e32 v164, v163
	v_pk_mul_f32 v[162:163], v[168:169], v[174:175]
	v_cvt_f32_ubyte0_e32 v2, v160
	v_pk_mul_f32 v[164:165], v[172:173], v[164:165]
	v_pk_mul_f32 v[22:23], v[22:23], v[162:163]
	v_rcp_iflag_f32_e32 v162, v2
	v_cvt_f32_ubyte0_e32 v2, v161
	v_pk_mul_f32 v[24:25], v[24:25], v[164:165]
	v_rcp_iflag_f32_e32 v164, v2
	v_cvt_f32_ubyte1_e32 v2, v160
	v_rcp_iflag_f32_e32 v163, v2
	v_cvt_f32_ubyte1_e32 v2, v161
	v_pk_mul_f32 v[166:167], v[166:167], v[176:177]
	v_rcp_iflag_f32_e32 v165, v2
	v_cvt_f32_ubyte2_e32 v2, v160
	v_pk_mul_f32 v[26:27], v[26:27], v[166:167]
	v_rcp_iflag_f32_e32 v166, v2
	v_cvt_f32_ubyte2_e32 v2, v161
	v_rcp_iflag_f32_e32 v168, v2
	v_cvt_f32_ubyte3_e32 v2, v160
	v_rcp_iflag_f32_e32 v167, v2
	v_cvt_f32_ubyte3_e32 v2, v161
	v_rcp_iflag_f32_e32 v169, v2
	v_pk_mul_f32 v[28:29], v[28:29], v[170:171]
	v_cvt_f32_ubyte3_e32 v171, v158
	v_cvt_f32_ubyte2_e32 v170, v158
	v_pk_mul_f32 v[166:167], v[166:167], v[170:171]
	v_cvt_f32_ubyte1_e32 v171, v159
	v_cvt_f32_ubyte0_e32 v170, v159
	v_cvt_f32_ubyte1_e32 v173, v158
	v_cvt_f32_ubyte0_e32 v172, v158
	v_cvt_f32_ubyte3_e32 v161, v159
	v_cvt_f32_ubyte2_e32 v160, v159
	v_pk_mul_f32 v[158:159], v[164:165], v[170:171]
	v_cvt_f32_ubyte0_e32 v2, v156
	v_pk_mul_f32 v[160:161], v[168:169], v[160:161]
	v_pk_mul_f32 v[14:15], v[14:15], v[158:159]
	v_rcp_iflag_f32_e32 v158, v2
	v_cvt_f32_ubyte0_e32 v2, v157
	v_pk_mul_f32 v[16:17], v[16:17], v[160:161]
	v_rcp_iflag_f32_e32 v160, v2
	v_cvt_f32_ubyte1_e32 v2, v156
	v_rcp_iflag_f32_e32 v159, v2
	v_cvt_f32_ubyte1_e32 v2, v157
	v_pk_mul_f32 v[162:163], v[162:163], v[172:173]
	v_rcp_iflag_f32_e32 v161, v2
	v_cvt_f32_ubyte2_e32 v2, v156
	v_pk_mul_f32 v[18:19], v[18:19], v[162:163]
	v_rcp_iflag_f32_e32 v162, v2
	v_cvt_f32_ubyte2_e32 v2, v157
	v_rcp_iflag_f32_e32 v164, v2
	v_cvt_f32_ubyte3_e32 v2, v156
	v_rcp_iflag_f32_e32 v163, v2
	v_cvt_f32_ubyte3_e32 v2, v157
	v_rcp_iflag_f32_e32 v165, v2
	v_pk_mul_f32 v[20:21], v[20:21], v[166:167]
	v_cvt_f32_ubyte3_e32 v167, v4
	v_cvt_f32_ubyte2_e32 v166, v4
	v_cvt_f32_ubyte1_e32 v169, v4
	v_cvt_f32_ubyte0_e32 v168, v4
	v_pk_mul_f32 v[162:163], v[162:163], v[166:167]
	v_cvt_f32_ubyte3_e32 v157, v5
	v_cvt_f32_ubyte2_e32 v156, v5
	v_cvt_f32_ubyte1_e32 v167, v5
	v_cvt_f32_ubyte0_e32 v166, v5
	v_pk_mul_f32 v[158:159], v[158:159], v[168:169]
	v_pk_mul_f32 v[4:5], v[160:161], v[166:167]
	v_pk_mul_f32 v[156:157], v[164:165], v[156:157]
	v_pk_mul_f32 v[12:13], v[12:13], v[162:163]
	v_pk_mul_f32 v[10:11], v[10:11], v[158:159]
	v_pk_mul_f32 v[8:9], v[8:9], v[156:157]
	v_pk_mul_f32 v[6:7], v[6:7], v[4:5]
	s_and_b64 vcc, exec, s[4:5]
	s_cbranch_vccz .LBB0_1604
	s_barrier

; __device__ __forceinline__ unsigned cvt_pk_bf16(float lo, float hi) { f32x2_t v = {lo, hi}; bf16x2_t b = __builtin_convertvector(v, bf16x2_t); return __builtin_bit_cast(unsigned, b); }
;     static __device__ __forceinline__ float ub(unsigned w, int k) { return (float)((w >> (8 * k)) & 0xffu); }
;     __device__ __forceinline__ void operator()(const f32x4 (&acc)[2][2][4][2], const Unit& u, int wr, int wc, int fr, int fq) const {
;         const int row0 = u.pm * BM + wr * 64 + fr, col0 = u.pn * BM + wc * 32 + 8 * fq;
;         const unsigned char* pa = g8 + ((size_t)3 * cfg::MT + row0) * cfg::DM + col0;
;         u32x2 ga[16];
; #pragma unroll
;         for (int i = 0; i < 16; ++i) ga[i] = *(const u32x2*)(pa + (size_t)(((i >> 3) & 1) * HALF + ((i >> 1) & 3) * 16) * cfg::DM + (i & 1) * HALF);
;         asm volatile("" ::: "memory");
; #pragma unroll
;         for (int i = 0; i < 16; ++i) { const int ai = (i >> 3) & 1, m = (i >> 1) & 3, bj = i & 1; const int r = row0 + ai * HALF + m * 16, c = col0 + bj * HALF;
;             f32x4 s0, s1;
; #pragma unroll
;             for (int j = 0; j < 4; ++j) { s0[j] = ub(ga[i].x, j) * (1.0f / 255.0f); s1[j] = ub(ga[i].y, j) * (1.0f / 255.0f); }
;             const f32x4 v0 = acc[ai][bj][m][0] * s0, v1 = acc[ai][bj][m][1] * s1;
;             u32x4 w; w.x = cvt_pk_bf16(v0[0], v0[1]); w.y = cvt_pk_bf16(v0[2], v0[3]); w.z = cvt_pk_bf16(v1[0], v1[1]); w.w = cvt_pk_bf16(v1[2], v1[3]);
;             *(u32x4*)(merged + (size_t)r * cfg::DM + c) = w; }
.LBB0_1608:
	v_add_u32_e32 v4, s24, v142
	v_ashrrev_i32_e32 v5, 31, v4
	v_or_b32_e32 v180, s26, v218
	v_ashrrev_i32_e32 v181, 31, v180
	s_lshl_b32 s2, s24, 12
	s_lshl_b32 s12, s26, 8
	s_add_i32 s2, s2, s12
	s_lshl_b32 s12, s39, 3
	s_add_i32 s2, s2, s12
	s_add_u32 s12, s6, 0x6001000
	s_addc_u32 s13, s7, 0
	s_add_u32 s12, s12, s2
	s_addc_u32 s13, s13, 0
	v_mbcnt_lo_u32_b32 v150, -1, 0
	v_mbcnt_hi_u32_b32 v150, -1, v150
	v_lshlrev_b32_e32 v150, 3, v150
	v_mov_b32_e32 v151, 0
	v_lshl_add_u64 v[150:151], s[12:13], 0, v[150:151]
	s_mov_b32 s22, 0x3b808081
	s_mov_b32 s2, 0x100000
	s_mov_b64 s[12:13], 0x100000
	global_load_dwordx2 v[182:183], v[150:151], off offset:-4096 nt
	global_load_dwordx2 v[178:179], v[150:151], off offset:-3584 nt
	global_load_dwordx2 v[176:177], v[150:151], off offset:-3072 nt
	global_load_dwordx2 v[174:175], v[150:151], off offset:-2560 nt
	global_load_dwordx2 v[172:173], v[150:151], off offset:-2048 nt
	global_load_dwordx2 v[170:171], v[150:151], off offset:-1536 nt
	global_load_dwordx2 v[168:169], v[150:151], off offset:-1024 nt
	global_load_dwordx2 v[166:167], v[150:151], off offset:-512 nt
	global_load_dwordx2 v[164:165], v[150:151], off nt
	global_load_dwordx2 v[162:163], v[150:151], off offset:512 nt
	global_load_dwordx2 v[160:161], v[150:151], off offset:1024 nt
	global_load_dwordx2 v[158:159], v[150:151], off offset:1536 nt
	global_load_dwordx2 v[156:157], v[150:151], off offset:2048 nt
	global_load_dwordx2 v[154:155], v[150:151], off offset:2560 nt
	global_load_dwordx2 v[152:153], v[150:151], off offset:3072 nt
	global_load_dwordx2 v[150:151], v[150:151], off offset:3584 nt
	s_waitcnt vmcnt(8)
	v_cvt_f32_ubyte1_e32 v187, v182
	v_cvt_f32_ubyte0_e32 v186, v182
	v_cvt_f32_ubyte3_e32 v185, v182
	v_cvt_f32_ubyte2_e32 v184, v182
	v_pk_mul_f32 v[186:187], v[186:187], s[22:23] op_sel_hi:[1,0]
	v_cvt_f32_ubyte3_e32 v189, v183
	v_cvt_f32_ubyte2_e32 v188, v183
	v_cvt_f32_ubyte1_e32 v191, v183
	v_cvt_f32_ubyte0_e32 v190, v183
	v_pk_mul_f32 v[184:185], v[184:185], s[22:23] op_sel_hi:[1,0]
	v_pk_mul_f32 v[182:183], v[190:191], s[22:23] op_sel_hi:[1,0]
	v_pk_mul_f32 v[188:189], v[188:189], s[22:23] op_sel_hi:[1,0]
	v_pk_mul_f32 v[130:131], v[130:131], v[186:187]
	v_pk_mul_f32 v[132:133], v[132:133], v[184:185]
	v_pk_mul_f32 v[184:185], v[128:129], v[188:189]
	v_pk_mul_f32 v[128:129], v[126:127], v[182:183]
	v_cvt_pk_bf16_f32 v126, v130, v131
	v_lshlrev_b64 v[130:131], 13, v[4:5]
	v_cvt_pk_bf16_f32 v127, v132, v133
	v_lshl_add_u64 v[132:133], s[8:9], 0, v[130:131]
	v_lshlrev_b64 v[130:131], 1, v[180:181]
	v_cvt_pk_bf16_f32 v128, v128, v129
	v_cvt_pk_bf16_f32 v129, v184, v185
	v_lshl_add_u64 v[132:133], v[132:133], 0, v[130:131]
	global_store_dwordx4 v[132:133], v[126:129], off
	v_cvt_f32_ubyte3_e32 v181, v179
	v_cvt_f32_ubyte2_e32 v180, v179
	v_cvt_f32_ubyte3_e32 v127, v178
	v_cvt_f32_ubyte2_e32 v126, v178
	v_cvt_f32_ubyte1_e32 v129, v178
	v_cvt_f32_ubyte0_e32 v128, v178
	v_cvt_f32_ubyte1_e32 v183, v179
	v_cvt_f32_ubyte0_e32 v182, v179
	v_pk_mul_f32 v[128:129], v[128:129], s[22:23] op_sel_hi:[1,0]
	v_pk_mul_f32 v[126:127], v[126:127], s[22:23] op_sel_hi:[1,0]
	v_pk_mul_f32 v[178:179], v[182:183], s[22:23] op_sel_hi:[1,0]
	v_pk_mul_f32 v[180:181], v[180:181], s[22:23] op_sel_hi:[1,0]
	v_pk_mul_f32 v[124:125], v[124:125], v[126:127]
	v_pk_mul_f32 v[122:123], v[122:123], v[128:129]
	v_pk_mul_f32 v[126:127], v[120:121], v[180:181]
	v_pk_mul_f32 v[120:121], v[118:119], v[178:179]
	v_cvt_pk_bf16_f32 v118, v122, v123
	v_cvt_pk_bf16_f32 v119, v124, v125
	v_cvt_pk_bf16_f32 v120, v120, v121
	v_cvt_pk_bf16_f32 v121, v126, v127
	global_store_dwordx4 v[132:133], v[118:121], off offset:256
	v_cvt_f32_ubyte3_e32 v123, v177
	v_cvt_f32_ubyte2_e32 v122, v177
	v_cvt_f32_ubyte1_e32 v121, v176
	v_cvt_f32_ubyte0_e32 v120, v176
	v_cvt_f32_ubyte3_e32 v119, v176
	v_cvt_f32_ubyte2_e32 v118, v176
	v_pk_mul_f32 v[120:121], v[120:121], s[22:23] op_sel_hi:[1,0]
	v_cvt_f32_ubyte1_e32 v125, v177
	v_cvt_f32_ubyte0_e32 v124, v177
	v_or_b32_e32 v126, 16, v4
	v_pk_mul_f32 v[118:119], v[118:119], s[22:23] op_sel_hi:[1,0]
	v_pk_mul_f32 v[124:125], v[124:125], s[22:23] op_sel_hi:[1,0]
	v_pk_mul_f32 v[122:123], v[122:123], s[22:23] op_sel_hi:[1,0]
	v_pk_mul_f32 v[114:115], v[114:115], v[120:121]
	v_ashrrev_i32_e32 v127, 31, v126
	v_pk_mul_f32 v[116:117], v[116:117], v[118:119]
	v_pk_mul_f32 v[118:119], v[112:113], v[122:123]
	v_pk_mul_f32 v[112:113], v[110:111], v[124:125]
	v_cvt_pk_bf16_f32 v110, v114, v115
	v_lshlrev_b64 v[114:115], 13, v[126:127]
	v_lshl_add_u64 v[114:115], s[8:9], 0, v[114:115]
	v_cvt_pk_bf16_f32 v111, v116, v117
	v_cvt_pk_bf16_f32 v112, v112, v113
	v_cvt_pk_bf16_f32 v113, v118, v119
	v_lshl_add_u64 v[114:115], v[114:115], 0, v[130:131]
	global_store_dwordx4 v[114:115], v[110:113], off
	v_cvt_f32_ubyte3_e32 v117, v175
	v_cvt_f32_ubyte2_e32 v116, v175
	v_cvt_f32_ubyte3_e32 v111, v174
	v_cvt_f32_ubyte2_e32 v110, v174
	v_cvt_f32_ubyte1_e32 v113, v174
	v_cvt_f32_ubyte0_e32 v112, v174
	v_cvt_f32_ubyte1_e32 v119, v175
	v_cvt_f32_ubyte0_e32 v118, v175
	v_pk_mul_f32 v[112:113], v[112:113], s[22:23] op_sel_hi:[1,0]
	v_pk_mul_f32 v[110:111], v[110:111], s[22:23] op_sel_hi:[1,0]
	v_pk_mul_f32 v[118:119], v[118:119], s[22:23] op_sel_hi:[1,0]
	v_pk_mul_f32 v[116:117], v[116:117], s[22:23] op_sel_hi:[1,0]
	v_pk_mul_f32 v[108:109], v[108:109], v[110:111]
	v_pk_mul_f32 v[106:107], v[106:107], v[112:113]
	v_pk_mul_f32 v[110:111], v[104:105], v[116:117]
	v_pk_mul_f32 v[104:105], v[102:103], v[118:119]
	v_cvt_pk_bf16_f32 v102, v106, v107
	v_cvt_pk_bf16_f32 v103, v108, v109
	v_cvt_pk_bf16_f32 v104, v104, v105
	v_cvt_pk_bf16_f32 v105, v110, v111
; __device__ __forceinline__ unsigned cvt_pk_bf16(float lo, float hi) { f32x2_t v = {lo, hi}; bf16x2_t b = __builtin_convertvector(v, bf16x2_t); return __builtin_bit_cast(unsigned, b); }
;     static __device__ __forceinline__ float ub(unsigned w, int k) { return (float)((w >> (8 * k)) & 0xffu); }
;     __device__ __forceinline__ void operator()(const f32x4 (&acc)[2][2][4][2], const Unit& u, int wr, int wc, int fr, int fq) const {
;     ...
; #pragma unroll
;         for (int i = 0; i < 16; ++i) { const int ai = (i >> 3) & 1, m = (i >> 1) & 3, bj = i & 1; const int r = row0 + ai * HALF + m * 16, c = col0 + bj * HALF;
;             f32x4 s0, s1;
; #pragma unroll
;             for (int j = 0; j < 4; ++j) { s0[j] = ub(ga[i].x, j) * (1.0f / 255.0f); s1[j] = ub(ga[i].y, j) * (1.0f / 255.0f); }
;             const f32x4 v0 = acc[ai][bj][m][0] * s0, v1 = acc[ai][bj][m][1] * s1;
;             u32x4 w; w.x = cvt_pk_bf16(v0[0], v0[1]); w.y = cvt_pk_bf16(v0[2], v0[3]); w.z = cvt_pk_bf16(v1[0], v1[1]); w.w = cvt_pk_bf16(v1[2], v1[3]);
;             *(u32x4*)(merged + (size_t)r * cfg::DM + c) = w; }
	global_store_dwordx4 v[114:115], v[102:105], off offset:256
	v_cvt_f32_ubyte3_e32 v107, v173
	v_cvt_f32_ubyte2_e32 v106, v173
	v_cvt_f32_ubyte1_e32 v105, v172
	v_cvt_f32_ubyte0_e32 v104, v172
	v_cvt_f32_ubyte3_e32 v103, v172
	v_cvt_f32_ubyte2_e32 v102, v172
	v_pk_mul_f32 v[104:105], v[104:105], s[22:23] op_sel_hi:[1,0]
	v_cvt_f32_ubyte1_e32 v109, v173
	v_cvt_f32_ubyte0_e32 v108, v173
	v_or_b32_e32 v110, 32, v4
	v_pk_mul_f32 v[102:103], v[102:103], s[22:23] op_sel_hi:[1,0]
	v_pk_mul_f32 v[108:109], v[108:109], s[22:23] op_sel_hi:[1,0]
	v_pk_mul_f32 v[106:107], v[106:107], s[22:23] op_sel_hi:[1,0]
	v_pk_mul_f32 v[98:99], v[98:99], v[104:105]
	v_ashrrev_i32_e32 v111, 31, v110
	v_pk_mul_f32 v[100:101], v[100:101], v[102:103]
	v_pk_mul_f32 v[102:103], v[96:97], v[106:107]
	v_pk_mul_f32 v[96:97], v[94:95], v[108:109]
	v_cvt_pk_bf16_f32 v94, v98, v99
	v_lshlrev_b64 v[98:99], 13, v[110:111]
	v_lshl_add_u64 v[98:99], s[8:9], 0, v[98:99]
	v_cvt_pk_bf16_f32 v95, v100, v101
	v_cvt_pk_bf16_f32 v96, v96, v97
	v_cvt_pk_bf16_f32 v97, v102, v103
	v_lshl_add_u64 v[98:99], v[98:99], 0, v[130:131]
	global_store_dwordx4 v[98:99], v[94:97], off
	v_cvt_f32_ubyte3_e32 v101, v171
	v_cvt_f32_ubyte2_e32 v100, v171
	v_cvt_f32_ubyte3_e32 v95, v170
	v_cvt_f32_ubyte2_e32 v94, v170
	v_cvt_f32_ubyte1_e32 v97, v170
	v_cvt_f32_ubyte0_e32 v96, v170
	v_cvt_f32_ubyte1_e32 v103, v171
	v_cvt_f32_ubyte0_e32 v102, v171
	v_pk_mul_f32 v[96:97], v[96:97], s[22:23] op_sel_hi:[1,0]
	v_pk_mul_f32 v[94:95], v[94:95], s[22:23] op_sel_hi:[1,0]
	v_pk_mul_f32 v[102:103], v[102:103], s[22:23] op_sel_hi:[1,0]
	v_pk_mul_f32 v[100:101], v[100:101], s[22:23] op_sel_hi:[1,0]
	v_pk_mul_f32 v[92:93], v[92:93], v[94:95]
	v_pk_mul_f32 v[90:91], v[90:91], v[96:97]
	v_pk_mul_f32 v[94:95], v[88:89], v[100:101]
	v_pk_mul_f32 v[88:89], v[86:87], v[102:103]
	v_cvt_pk_bf16_f32 v86, v90, v91
	v_cvt_pk_bf16_f32 v87, v92, v93
	v_cvt_pk_bf16_f32 v88, v88, v89
	v_cvt_pk_bf16_f32 v89, v94, v95
	global_store_dwordx4 v[98:99], v[86:89], off offset:256
	v_cvt_f32_ubyte3_e32 v91, v169
	v_cvt_f32_ubyte2_e32 v90, v169
	v_cvt_f32_ubyte1_e32 v89, v168
	v_cvt_f32_ubyte0_e32 v88, v168
	v_cvt_f32_ubyte3_e32 v87, v168
	v_cvt_f32_ubyte2_e32 v86, v168
	v_pk_mul_f32 v[88:89], v[88:89], s[22:23] op_sel_hi:[1,0]
	v_cvt_f32_ubyte1_e32 v93, v169
	v_cvt_f32_ubyte0_e32 v92, v169
	v_or_b32_e32 v94, 48, v4
	v_pk_mul_f32 v[86:87], v[86:87], s[22:23] op_sel_hi:[1,0]
	v_pk_mul_f32 v[92:93], v[92:93], s[22:23] op_sel_hi:[1,0]
	v_pk_mul_f32 v[90:91], v[90:91], s[22:23] op_sel_hi:[1,0]
	v_pk_mul_f32 v[82:83], v[82:83], v[88:89]
	v_ashrrev_i32_e32 v95, 31, v94
	v_pk_mul_f32 v[84:85], v[84:85], v[86:87]
	v_pk_mul_f32 v[86:87], v[80:81], v[90:91]
	v_pk_mul_f32 v[80:81], v[78:79], v[92:93]
	v_cvt_pk_bf16_f32 v78, v82, v83
	v_lshlrev_b64 v[82:83], 13, v[94:95]
	v_lshl_add_u64 v[82:83], s[8:9], 0, v[82:83]
	v_cvt_pk_bf16_f32 v79, v84, v85
	v_cvt_pk_bf16_f32 v80, v80, v81
	v_cvt_pk_bf16_f32 v81, v86, v87
	v_lshl_add_u64 v[82:83], v[82:83], 0, v[130:131]
	global_store_dwordx4 v[82:83], v[78:81], off
	v_cvt_f32_ubyte3_e32 v85, v167
	v_cvt_f32_ubyte2_e32 v84, v167
	v_cvt_f32_ubyte3_e32 v79, v166
	v_cvt_f32_ubyte2_e32 v78, v166
	v_cvt_f32_ubyte1_e32 v81, v166
	v_cvt_f32_ubyte0_e32 v80, v166
	v_cvt_f32_ubyte1_e32 v87, v167
	v_cvt_f32_ubyte0_e32 v86, v167
	v_pk_mul_f32 v[80:81], v[80:81], s[22:23] op_sel_hi:[1,0]
	v_pk_mul_f32 v[78:79], v[78:79], s[22:23] op_sel_hi:[1,0]
	v_pk_mul_f32 v[86:87], v[86:87], s[22:23] op_sel_hi:[1,0]
	v_pk_mul_f32 v[84:85], v[84:85], s[22:23] op_sel_hi:[1,0]
	v_pk_mul_f32 v[76:77], v[76:77], v[78:79]
	v_pk_mul_f32 v[74:75], v[74:75], v[80:81]
	v_pk_mul_f32 v[78:79], v[72:73], v[84:85]
	v_pk_mul_f32 v[72:73], v[70:71], v[86:87]
	v_cvt_pk_bf16_f32 v70, v74, v75
	v_cvt_pk_bf16_f32 v71, v76, v77
	v_cvt_pk_bf16_f32 v72, v72, v73
	v_cvt_pk_bf16_f32 v73, v78, v79
	global_store_dwordx4 v[82:83], v[70:73], off offset:256
	s_waitcnt vmcnt(15)
	v_cvt_f32_ubyte3_e32 v75, v165
	v_cvt_f32_ubyte2_e32 v74, v165
	v_cvt_f32_ubyte3_e32 v71, v164
	v_cvt_f32_ubyte2_e32 v70, v164
	v_cvt_f32_ubyte1_e32 v73, v164
	v_cvt_f32_ubyte0_e32 v72, v164
	v_pk_mul_f32 v[70:71], v[70:71], s[22:23] op_sel_hi:[1,0]
	v_cvt_f32_ubyte1_e32 v77, v165
	v_cvt_f32_ubyte0_e32 v76, v165
	v_pk_mul_f32 v[72:73], v[72:73], s[22:23] op_sel_hi:[1,0]
	v_pk_mul_f32 v[76:77], v[76:77], s[22:23] op_sel_hi:[1,0]
	v_pk_mul_f32 v[74:75], v[74:75], s[22:23] op_sel_hi:[1,0]
	v_pk_mul_f32 v[68:69], v[68:69], v[70:71]
	v_pk_mul_f32 v[66:67], v[66:67], v[72:73]
	v_pk_mul_f32 v[70:71], v[64:65], v[74:75]
	v_pk_mul_f32 v[64:65], v[62:63], v[76:77]
	v_cvt_pk_bf16_f32 v63, v68, v69
	v_add_co_u32_e32 v68, vcc, s2, v132
	v_cvt_pk_bf16_f32 v62, v66, v67
	v_cvt_pk_bf16_f32 v64, v64, v65
	v_cvt_pk_bf16_f32 v65, v70, v71
	v_addc_co_u32_e32 v69, vcc, 0, v133, vcc
	global_store_dwordx4 v[68:69], v[62:65], off
	s_waitcnt vmcnt(15)
	v_cvt_f32_ubyte3_e32 v69, v163
	v_cvt_f32_ubyte2_e32 v68, v163
	v_cvt_f32_ubyte3_e32 v63, v162
	v_cvt_f32_ubyte2_e32 v62, v162
	v_cvt_f32_ubyte1_e32 v65, v162
	v_cvt_f32_ubyte0_e32 v64, v162
	v_cvt_f32_ubyte1_e32 v71, v163
	v_cvt_f32_ubyte0_e32 v70, v163
	v_pk_mul_f32 v[64:65], v[64:65], s[22:23] op_sel_hi:[1,0]
	v_pk_mul_f32 v[62:63], v[62:63], s[22:23] op_sel_hi:[1,0]
	v_pk_mul_f32 v[70:71], v[70:71], s[22:23] op_sel_hi:[1,0]
	v_pk_mul_f32 v[68:69], v[68:69], s[22:23] op_sel_hi:[1,0]
	v_pk_mul_f32 v[60:61], v[60:61], v[62:63]
	v_pk_mul_f32 v[58:59], v[58:59], v[64:65]
	v_pk_mul_f32 v[62:63], v[56:57], v[68:69]
	v_pk_mul_f32 v[56:57], v[54:55], v[70:71]
	v_lshl_add_u64 v[66:67], v[132:133], 0, s[12:13]
	v_cvt_pk_bf16_f32 v54, v58, v59
	v_cvt_pk_bf16_f32 v55, v60, v61
	v_cvt_pk_bf16_f32 v56, v56, v57
	v_cvt_pk_bf16_f32 v57, v62, v63
	global_store_dwordx4 v[66:67], v[54:57], off offset:256
	s_waitcnt vmcnt(15)
; __device__ __forceinline__ unsigned cvt_pk_bf16(float lo, float hi) { f32x2_t v = {lo, hi}; bf16x2_t b = __builtin_convertvector(v, bf16x2_t); return __builtin_bit_cast(unsigned, b); }
;     static __device__ __forceinline__ float ub(unsigned w, int k) { return (float)((w >> (8 * k)) & 0xffu); }
; #define PG8_BAR __builtin_amdgcn_s_barrier()
;     __device__ __forceinline__ void operator()(const f32x4 (&acc)[2][2][4][2], const Unit& u, int wr, int wc, int fr, int fq) const {
;     ...
; #pragma unroll
;         for (int i = 0; i < 16; ++i) { const int ai = (i >> 3) & 1, m = (i >> 1) & 3, bj = i & 1; const int r = row0 + ai * HALF + m * 16, c = col0 + bj * HALF;
;             f32x4 s0, s1;
; #pragma unroll
;             for (int j = 0; j < 4; ++j) { s0[j] = ub(ga[i].x, j) * (1.0f / 255.0f); s1[j] = ub(ga[i].y, j) * (1.0f / 255.0f); }
;             const f32x4 v0 = acc[ai][bj][m][0] * s0, v1 = acc[ai][bj][m][1] * s1;
;             u32x4 w; w.x = cvt_pk_bf16(v0[0], v0[1]); w.y = cvt_pk_bf16(v0[2], v0[3]); w.z = cvt_pk_bf16(v1[0], v1[1]); w.w = cvt_pk_bf16(v1[2], v1[3]);
;             *(u32x4*)(merged + (size_t)r * cfg::DM + c) = w; }
; template <class Epi, class Sched, bool ALIGN_EPI = false, bool SP2 = false>
; __device__ __forceinline__ void gemm_phase(PG8_LAS unsigned char* lds, const Gemm g, const Sched& S, const Epi& E) {
;     ...
;         if constexpr (ALIGN_EPI) { if (wr == 0) PG8_BAR; }
;         if constexpr (!Epi::AFTER_DRAIN) { E(acc, cur, wr, wc, fr, fq); S.done(cur); }
;         if (!has_next) break;
; #pragma unroll
;         for (int a = 0; a < 2; ++a)
; #pragma unroll
;             for (int b = 0; b < 2; ++b)
; #pragma unroll
;                 for (int m = 0; m < 4; ++m)
; #pragma unroll
;                     for (int n = 0; n < 2; ++n) acc[a][b][m][n] = (f32x4){0.f, 0.f, 0.f, 0.f};
;         cur = nxt; cA = nA; cB = nB; ++ui;
;         if constexpr (ALIGN_EPI) { if (wr == 1) PG8_BAR; }
	v_cvt_f32_ubyte3_e32 v59, v161
	v_cvt_f32_ubyte2_e32 v58, v161
	v_cvt_f32_ubyte1_e32 v57, v160
	v_cvt_f32_ubyte0_e32 v56, v160
	v_cvt_f32_ubyte3_e32 v55, v160
	v_cvt_f32_ubyte2_e32 v54, v160
	v_pk_mul_f32 v[56:57], v[56:57], s[22:23] op_sel_hi:[1,0]
	v_cvt_f32_ubyte1_e32 v61, v161
	v_cvt_f32_ubyte0_e32 v60, v161
	v_add_u32_e32 v62, 0x90, v4
	v_pk_mul_f32 v[54:55], v[54:55], s[22:23] op_sel_hi:[1,0]
	v_pk_mul_f32 v[60:61], v[60:61], s[22:23] op_sel_hi:[1,0]
	v_pk_mul_f32 v[58:59], v[58:59], s[22:23] op_sel_hi:[1,0]
	v_pk_mul_f32 v[50:51], v[50:51], v[56:57]
	v_ashrrev_i32_e32 v63, 31, v62
	v_pk_mul_f32 v[52:53], v[52:53], v[54:55]
	v_pk_mul_f32 v[54:55], v[48:49], v[58:59]
	v_pk_mul_f32 v[48:49], v[46:47], v[60:61]
	v_cvt_pk_bf16_f32 v46, v50, v51
	v_lshlrev_b64 v[50:51], 13, v[62:63]
	v_lshl_add_u64 v[50:51], s[8:9], 0, v[50:51]
	v_cvt_pk_bf16_f32 v47, v52, v53
	v_cvt_pk_bf16_f32 v48, v48, v49
	v_cvt_pk_bf16_f32 v49, v54, v55
	v_lshl_add_u64 v[50:51], v[50:51], 0, v[130:131]
	global_store_dwordx4 v[50:51], v[46:49], off
	s_waitcnt vmcnt(15)
	v_cvt_f32_ubyte3_e32 v53, v159
	v_cvt_f32_ubyte2_e32 v52, v159
	v_cvt_f32_ubyte3_e32 v47, v158
	v_cvt_f32_ubyte2_e32 v46, v158
	v_cvt_f32_ubyte1_e32 v49, v158
	v_cvt_f32_ubyte0_e32 v48, v158
	v_cvt_f32_ubyte1_e32 v55, v159
	v_cvt_f32_ubyte0_e32 v54, v159
	v_pk_mul_f32 v[48:49], v[48:49], s[22:23] op_sel_hi:[1,0]
	v_pk_mul_f32 v[46:47], v[46:47], s[22:23] op_sel_hi:[1,0]
	v_pk_mul_f32 v[54:55], v[54:55], s[22:23] op_sel_hi:[1,0]
	v_pk_mul_f32 v[52:53], v[52:53], s[22:23] op_sel_hi:[1,0]
	v_pk_mul_f32 v[44:45], v[44:45], v[46:47]
	v_pk_mul_f32 v[42:43], v[42:43], v[48:49]
	v_pk_mul_f32 v[46:47], v[40:41], v[52:53]
	v_pk_mul_f32 v[40:41], v[38:39], v[54:55]
	v_cvt_pk_bf16_f32 v38, v42, v43
	v_cvt_pk_bf16_f32 v39, v44, v45
	v_cvt_pk_bf16_f32 v40, v40, v41
	v_cvt_pk_bf16_f32 v41, v46, v47
	global_store_dwordx4 v[50:51], v[38:41], off offset:256
	s_waitcnt vmcnt(15)
	v_cvt_f32_ubyte3_e32 v43, v157
	v_cvt_f32_ubyte2_e32 v42, v157
	v_cvt_f32_ubyte1_e32 v41, v156
	v_cvt_f32_ubyte0_e32 v40, v156
	v_cvt_f32_ubyte3_e32 v39, v156
	v_cvt_f32_ubyte2_e32 v38, v156
	v_pk_mul_f32 v[40:41], v[40:41], s[22:23] op_sel_hi:[1,0]
	v_cvt_f32_ubyte1_e32 v45, v157
	v_cvt_f32_ubyte0_e32 v44, v157
	v_add_u32_e32 v46, 0xa0, v4
	v_pk_mul_f32 v[38:39], v[38:39], s[22:23] op_sel_hi:[1,0]
	v_pk_mul_f32 v[44:45], v[44:45], s[22:23] op_sel_hi:[1,0]
	v_pk_mul_f32 v[42:43], v[42:43], s[22:23] op_sel_hi:[1,0]
	v_pk_mul_f32 v[34:35], v[34:35], v[40:41]
	v_ashrrev_i32_e32 v47, 31, v46
	v_pk_mul_f32 v[36:37], v[36:37], v[38:39]
	v_pk_mul_f32 v[38:39], v[32:33], v[42:43]
	v_pk_mul_f32 v[32:33], v[30:31], v[44:45]
	v_cvt_pk_bf16_f32 v30, v34, v35
	v_lshlrev_b64 v[34:35], 13, v[46:47]
	v_lshl_add_u64 v[34:35], s[8:9], 0, v[34:35]
	v_cvt_pk_bf16_f32 v31, v36, v37
	v_cvt_pk_bf16_f32 v32, v32, v33
	v_cvt_pk_bf16_f32 v33, v38, v39
	v_lshl_add_u64 v[34:35], v[34:35], 0, v[130:131]
	global_store_dwordx4 v[34:35], v[30:33], off
	s_waitcnt vmcnt(15)
	v_cvt_f32_ubyte3_e32 v37, v155
	v_cvt_f32_ubyte2_e32 v36, v155
	v_cvt_f32_ubyte3_e32 v31, v154
	v_cvt_f32_ubyte2_e32 v30, v154
	v_cvt_f32_ubyte1_e32 v33, v154
	v_cvt_f32_ubyte0_e32 v32, v154
	v_cvt_f32_ubyte1_e32 v39, v155
	v_cvt_f32_ubyte0_e32 v38, v155
	v_pk_mul_f32 v[32:33], v[32:33], s[22:23] op_sel_hi:[1,0]
	v_pk_mul_f32 v[30:31], v[30:31], s[22:23] op_sel_hi:[1,0]
	v_pk_mul_f32 v[38:39], v[38:39], s[22:23] op_sel_hi:[1,0]
	v_pk_mul_f32 v[36:37], v[36:37], s[22:23] op_sel_hi:[1,0]
	v_pk_mul_f32 v[28:29], v[28:29], v[30:31]
	v_pk_mul_f32 v[26:27], v[26:27], v[32:33]
	v_pk_mul_f32 v[30:31], v[24:25], v[36:37]
	v_pk_mul_f32 v[24:25], v[22:23], v[38:39]
	v_cvt_pk_bf16_f32 v22, v26, v27
	v_cvt_pk_bf16_f32 v23, v28, v29
	v_cvt_pk_bf16_f32 v24, v24, v25
	v_cvt_pk_bf16_f32 v25, v30, v31
	v_add_u32_e32 v4, 0xb0, v4
	global_store_dwordx4 v[34:35], v[22:25], off offset:256
	s_waitcnt vmcnt(15)
	v_cvt_f32_ubyte3_e32 v27, v153
	v_cvt_f32_ubyte2_e32 v26, v153
	v_cvt_f32_ubyte3_e32 v23, v152
	v_cvt_f32_ubyte2_e32 v22, v152
	v_cvt_f32_ubyte1_e32 v25, v152
	v_cvt_f32_ubyte0_e32 v24, v152
	v_cvt_f32_ubyte1_e32 v29, v153
	v_cvt_f32_ubyte0_e32 v28, v153
	v_ashrrev_i32_e32 v5, 31, v4
	v_pk_mul_f32 v[24:25], v[24:25], s[22:23] op_sel_hi:[1,0]
	v_pk_mul_f32 v[22:23], v[22:23], s[22:23] op_sel_hi:[1,0]
	v_pk_mul_f32 v[28:29], v[28:29], s[22:23] op_sel_hi:[1,0]
	v_pk_mul_f32 v[26:27], v[26:27], s[22:23] op_sel_hi:[1,0]
	v_lshlrev_b64 v[4:5], 13, v[4:5]
	v_pk_mul_f32 v[20:21], v[20:21], v[22:23]
	v_pk_mul_f32 v[18:19], v[18:19], v[24:25]
	v_pk_mul_f32 v[22:23], v[16:17], v[26:27]
	v_pk_mul_f32 v[16:17], v[14:15], v[28:29]
	v_lshl_add_u64 v[4:5], s[8:9], 0, v[4:5]
	v_cvt_pk_bf16_f32 v14, v18, v19
	v_cvt_pk_bf16_f32 v15, v20, v21
	v_cvt_pk_bf16_f32 v16, v16, v17
	v_cvt_pk_bf16_f32 v17, v22, v23
	v_lshl_add_u64 v[18:19], v[4:5], 0, v[130:131]
	global_store_dwordx4 v[18:19], v[14:17], off
	s_waitcnt vmcnt(15)
	v_cvt_f32_ubyte3_e32 v5, v150
	v_cvt_f32_ubyte2_e32 v4, v150
	v_cvt_f32_ubyte1_e32 v15, v150
	v_cvt_f32_ubyte0_e32 v14, v150
	v_cvt_f32_ubyte3_e32 v17, v151
	v_cvt_f32_ubyte2_e32 v16, v151
	v_cvt_f32_ubyte1_e32 v21, v151
	v_cvt_f32_ubyte0_e32 v20, v151
	v_pk_mul_f32 v[14:15], v[14:15], s[22:23] op_sel_hi:[1,0]
	v_pk_mul_f32 v[4:5], v[4:5], s[22:23] op_sel_hi:[1,0]
	v_pk_mul_f32 v[20:21], v[20:21], s[22:23] op_sel_hi:[1,0]
	v_pk_mul_f32 v[16:17], v[16:17], s[22:23] op_sel_hi:[1,0]
	v_pk_mul_f32 v[12:13], v[12:13], v[4:5]
	v_pk_mul_f32 v[4:5], v[10:11], v[14:15]
	v_pk_mul_f32 v[8:9], v[8:9], v[16:17]
	v_pk_mul_f32 v[6:7], v[6:7], v[20:21]
	v_cvt_pk_bf16_f32 v4, v4, v5
	v_cvt_pk_bf16_f32 v5, v12, v13
	v_cvt_pk_bf16_f32 v6, v6, v7
	v_cvt_pk_bf16_f32 v7, v8, v9
	s_mov_b64 s[12:13], -1
	s_andn2_b64 vcc, exec, s[0:1]
	global_store_dwordx4 v[18:19], v[4:7], off offset:256
	s_cbranch_vccnz .LBB0_1594
	s_andn2_b64 vcc, exec, s[4:5]
	s_cbranch_vccnz .LBB0_1593
	s_barrier
	s_branch .LBB0_1593
